# hybrid K1 ring 32: queue flushed once at the private->shared transition (about 3/4 of the entries, one chunk of slack), rest at wave end
# baseline (speedup 1.0000x reference)
.Lk1_cskip_m:
	s_cmp_eq_u32 s26, 6
	s_cbranch_scc1 .Lk1_pfo_go
	s_cmp_eq_u32 s26, 7
	s_cbranch_scc0 .Lk1_pfo_skip

.Lk1_inone_m:
.Lk1_pfo_skip:
	s_waitcnt vmcnt(31)
	v_or3_b32 v12, v28, v29, v30
	v_or_b32_e32 v12, v12, v31
	v_cmp_ne_u32_e32 vcc, 0, v12
	s_cbranch_vccnz .Lk1_hitm_0
